# A8: attention loops - the 31 row-sum adds moved from between the last MFMA and BAR#2 into the shadow of the 16 P*V MFMAs (loop-free temporaries, same summation order); on top of A5-A7+T4+A4+O1+T1-T3+G
# speedup vs baseline: 1.0018x; 1.0018x over previous
.LBB0_859:
	s_setprio 1
	v_add_u32_e32 v170, s94, v215
	v_add_u32_e32 v76, v170, v216
	ds_read_b128 v[64:67], v76 offset:0
	ds_read_b128 v[68:71], v76 offset:0x1000
	ds_read_b128 v[72:75], v76 offset:0x2000
	ds_read_b128 v[76:79], v76 offset:0x3000
	v_add_u32_e32 v171, v170, v217
	s_waitcnt lgkmcnt(3)
	s_cmp_gt_i32 s67, -1
	v_mfma_f32_32x32x16_bf16 v[80:95], v[64:67], v[12:15], v[80:95]
	v_add_f32_e32 v246, v96, v112
	ds_read_b128 v[64:67], v171 offset:0
	s_waitcnt lgkmcnt(3)
	s_cselect_b64 s[80:81], -1, 0
	s_cmp_lt_i32 s67, 0
	s_cselect_b64 s[88:89], -1, 0
	s_and_b64 vcc, exec, s[88:89]
	v_mfma_f32_32x32x16_bf16 v[48:63], v[68:71], v[12:15], v[48:63]
	v_add_f32_e32 v248, v97, v113
	v_add_f32_e32 v246, v248, v246
	ds_read_b128 v[68:71], v171 offset:0x1000
	s_waitcnt lgkmcnt(3)
	s_nop 0
	v_mfma_f32_32x32x16_bf16 v[32:47], v[72:75], v[12:15], v[32:47]
	v_add_f32_e32 v247, v98, v114
	v_add_f32_e32 v246, v247, v246
	ds_read_b128 v[72:75], v171 offset:0x2000
	s_waitcnt lgkmcnt(3)
	s_nop 0
	v_mfma_f32_32x32x16_bf16 v[16:31], v[76:79], v[12:15], v[16:31]
	v_add_f32_e32 v248, v99, v115
	v_add_f32_e32 v246, v248, v246
	ds_read_b128 v[12:15], v171 offset:0x3000
	s_waitcnt lgkmcnt(3)
	v_add_u32_e32 v76, v170, v218
	v_mfma_f32_32x32x16_bf16 v[80:95], v[64:67], v[8:11], v[80:95]
	v_add_f32_e32 v247, v100, v116
	v_add_f32_e32 v246, v247, v246
	ds_read_b128 v[64:67], v76 offset:0
	s_waitcnt lgkmcnt(3)
	s_nop 0
	v_mfma_f32_32x32x16_bf16 v[48:63], v[68:71], v[8:11], v[48:63]
	v_add_f32_e32 v248, v101, v117
	v_add_f32_e32 v246, v248, v246
	ds_read_b128 v[68:71], v76 offset:0x1000
	s_waitcnt lgkmcnt(3)
	s_nop 0
	v_mfma_f32_32x32x16_bf16 v[32:47], v[72:75], v[8:11], v[32:47]
	v_add_f32_e32 v247, v102, v118
	v_add_f32_e32 v246, v247, v246
	ds_read_b128 v[72:75], v76 offset:0x2000
	s_waitcnt lgkmcnt(3)
	s_nop 0
	v_mfma_f32_32x32x16_bf16 v[16:31], v[12:15], v[8:11], v[16:31]
	v_add_f32_e32 v248, v103, v119
	v_add_f32_e32 v246, v248, v246
	ds_read_b128 v[8:11], v76 offset:0x3000
	s_waitcnt lgkmcnt(3)
	v_add_u32_e32 v76, v170, v219
	ds_read_b128 v[12:15], v76 offset:0
	s_waitcnt lgkmcnt(3)
	v_mfma_f32_32x32x16_bf16 v[80:95], v[64:67], v[4:7], v[80:95]
	v_add_f32_e32 v247, v104, v120
	v_add_f32_e32 v246, v247, v246
	ds_read_b128 v[64:67], v76 offset:0x1000
	s_waitcnt lgkmcnt(3)
	v_mfma_f32_32x32x16_bf16 v[48:63], v[68:71], v[4:7], v[48:63]
	v_add_f32_e32 v248, v105, v121
	v_add_f32_e32 v246, v248, v246
	ds_read_b128 v[68:71], v76 offset:0x2000
	s_waitcnt lgkmcnt(3)
	v_mfma_f32_32x32x16_bf16 v[32:47], v[72:75], v[4:7], v[32:47]
	v_add_f32_e32 v247, v106, v122
	v_add_f32_e32 v246, v247, v246
	v_mfma_f32_32x32x16_bf16 v[16:31], v[8:11], v[4:7], v[16:31]
	v_add_f32_e32 v248, v107, v123
	v_add_f32_e32 v246, v248, v246
	ds_read_b128 v[4:7], v76 offset:0x3000
	s_waitcnt lgkmcnt(3)
	s_waitcnt lgkmcnt(2)
	s_waitcnt lgkmcnt(1)
	s_nop 0
	s_waitcnt lgkmcnt(0)
	v_mfma_f32_32x32x16_bf16 v[80:95], v[12:15], v[0:3], v[80:95]
	v_add_f32_e32 v247, v108, v124
	v_add_f32_e32 v246, v247, v246
	v_mfma_f32_32x32x16_bf16 v[48:63], v[64:67], v[0:3], v[48:63]
	v_add_f32_e32 v248, v109, v125
	v_add_f32_e32 v246, v248, v246
	v_mfma_f32_32x32x16_bf16 v[32:47], v[68:71], v[0:3], v[32:47]
	v_add_f32_e32 v247, v110, v126
	v_add_f32_e32 v246, v247, v246
	v_mfma_f32_32x32x16_bf16 v[16:31], v[4:7], v[0:3], v[16:31]
	v_add_f32_e32 v248, v111, v127
	v_add_f32_e32 v246, v248, v246
	s_cbranch_vccnz .LBB0_861
	s_add_i32 s68, s94, 0x8000
	s_and_b32 s68, s68, 0x18000
	v_add_u32_e32 v170, s68, v167
	v_add_u32_e32 v4, v170, v207
	ds_read_b128 v[0:3], v4 offset:0
	ds_read_b128 v[4:7], v4 offset:0x2000
	v_add_u32_e32 v8, v170, v208
	ds_read_b128 v[230:233], v8 offset:0
	ds_read_b128 v[234:237], v8 offset:0x2000
	s_waitcnt lgkmcnt(3)
	v_add_u32_e32 v171, v170, v209
	ds_read_b128 v[238:241], v171 offset:0
	v_mfma_f32_32x32x16_bf16 v[64:79], v[0:3], v[128:131], 0
	s_waitcnt lgkmcnt(3)
	ds_read_b128 v[242:245], v171 offset:0x2000
	s_waitcnt lgkmcnt(3)
	v_add_u32_e32 v171, v170, v210
	v_mfma_f32_32x32x16_bf16 v[0:15], v[4:7], v[128:131], 0
	v_mfma_f32_32x32x16_bf16 v[64:79], v[230:233], v[132:135], v[64:79]
	ds_read_b128 v[230:233], v171 offset:0
	s_waitcnt lgkmcnt(3)
	s_nop 0
	v_mfma_f32_32x32x16_bf16 v[0:15], v[234:237], v[132:135], v[0:15]
	ds_read_b128 v[234:237], v171 offset:0x2000
	s_waitcnt lgkmcnt(3)
	v_add_u32_e32 v171, v170, v211
	v_mfma_f32_32x32x16_bf16 v[64:79], v[238:241], v[136:139], v[64:79]
	ds_read_b128 v[238:241], v171 offset:0
	s_waitcnt lgkmcnt(3)
	s_nop 0
	v_mfma_f32_32x32x16_bf16 v[0:15], v[242:245], v[136:139], v[0:15]
	ds_read_b128 v[242:245], v171 offset:0x2000
	s_waitcnt lgkmcnt(3)
	v_add_u32_e32 v171, v170, v212
	v_mfma_f32_32x32x16_bf16 v[64:79], v[230:233], v[140:143], v[64:79]
	ds_read_b128 v[230:233], v171 offset:0
	s_waitcnt lgkmcnt(3)
	s_nop 0
	v_mfma_f32_32x32x16_bf16 v[0:15], v[234:237], v[140:143], v[0:15]
	ds_read_b128 v[234:237], v171 offset:0x2000
	s_waitcnt lgkmcnt(3)
	v_add_u32_e32 v171, v170, v213
	v_add_u32_e32 v170, v170, v214
	v_mfma_f32_32x32x16_bf16 v[64:79], v[238:241], v[144:147], v[64:79]
	ds_read_b128 v[238:241], v171 offset:0
	s_waitcnt lgkmcnt(3)
	s_nop 0
	v_mfma_f32_32x32x16_bf16 v[0:15], v[242:245], v[144:147], v[0:15]
	ds_read_b128 v[242:245], v171 offset:0x2000
	s_waitcnt lgkmcnt(3)
	s_nop 0
	v_mfma_f32_32x32x16_bf16 v[64:79], v[230:233], v[148:151], v[64:79]
	ds_read_b128 v[230:233], v170 offset:0
	s_waitcnt lgkmcnt(3)
	s_nop 0
	v_mfma_f32_32x32x16_bf16 v[0:15], v[234:237], v[148:151], v[0:15]
	ds_read_b128 v[234:237], v170 offset:0x2000
	s_waitcnt lgkmcnt(3)
	s_waitcnt lgkmcnt(2)
	s_waitcnt lgkmcnt(1)
	s_nop 0
	s_waitcnt lgkmcnt(0)
	v_mfma_f32_32x32x16_bf16 v[64:79], v[238:241], v[152:155], v[64:79]
	v_mfma_f32_32x32x16_bf16 v[0:15], v[242:245], v[152:155], v[0:15]
	v_mfma_f32_32x32x16_bf16 v[64:79], v[230:233], v[156:159], v[64:79]
	v_mfma_f32_32x32x16_bf16 v[0:15], v[234:237], v[156:159], v[0:15]
	s_setprio 0
	s_and_b64 vcc, exec, s[0:1]
	s_cbranch_vccz .LBB0_862
	s_branch .LBB0_866

.LBB0_866:
	s_barrier
	v_add_f32_e32 v228, v228, v246
	s_andn2_b64 vcc, exec, s[80:81]
	s_cbranch_vccnz .LBB0_847
	s_cmp_lg_u32 s67, s66
	s_cbranch_scc0 .LBB0_872
	v_lshrrev_b64 v[96:97], s67, v[182:183]
	v_and_b32_e32 v96, 1, v96
	v_cmp_ne_u32_e64 s[74:75], 0, v96
	v_mov_b64_e32 v[126:127], v[78:79]
	v_cmp_eq_u32_e32 vcc, 1, v96
	s_mov_b64 s[80:81], 0
	s_cmp_lg_u64 s[74:75], exec
	v_mov_b64_e32 v[124:125], v[76:77]
	v_mov_b64_e32 v[122:123], v[74:75]
	v_mov_b64_e32 v[120:121], v[72:73]
	v_mov_b64_e32 v[118:119], v[70:71]
	v_mov_b64_e32 v[116:117], v[68:69]
	v_mov_b64_e32 v[114:115], v[66:67]
	v_mov_b64_e32 v[112:113], v[64:65]
	s_mov_b64 s[74:75], 0
	s_cbranch_scc0 .LBB0_870
	v_cndmask_b32_e32 v112, v203, v64, vcc
	v_cndmask_b32_e32 v96, v203, v0, vcc
	v_cndmask_b32_e32 v113, v203, v65, vcc
	v_cndmask_b32_e32 v97, v203, v1, vcc
	v_cndmask_b32_e32 v114, v203, v66, vcc
	v_cndmask_b32_e32 v98, v203, v2, vcc
	v_cndmask_b32_e32 v115, v203, v67, vcc
	v_cndmask_b32_e32 v99, v203, v3, vcc
	v_cndmask_b32_e32 v116, v203, v68, vcc
	v_cndmask_b32_e32 v100, v203, v4, vcc
	v_cndmask_b32_e32 v117, v203, v69, vcc
	v_cndmask_b32_e32 v101, v203, v5, vcc
	v_cndmask_b32_e32 v118, v203, v70, vcc
	v_cndmask_b32_e32 v102, v203, v6, vcc
	v_cndmask_b32_e32 v119, v203, v71, vcc
	v_cndmask_b32_e32 v103, v203, v7, vcc
	v_cndmask_b32_e32 v120, v203, v72, vcc
	v_cndmask_b32_e32 v104, v203, v8, vcc
	v_cndmask_b32_e32 v121, v203, v73, vcc
	v_cndmask_b32_e32 v105, v203, v9, vcc
	v_cndmask_b32_e32 v122, v203, v74, vcc
	v_cndmask_b32_e32 v106, v203, v10, vcc
	v_cndmask_b32_e32 v123, v203, v75, vcc
	v_cndmask_b32_e32 v107, v203, v11, vcc
	v_cndmask_b32_e32 v124, v203, v76, vcc
	v_cndmask_b32_e32 v108, v203, v12, vcc
	v_cndmask_b32_e32 v125, v203, v77, vcc
	v_cndmask_b32_e32 v109, v203, v13, vcc
	v_cndmask_b32_e32 v126, v203, v78, vcc
	v_cndmask_b32_e32 v110, v203, v14, vcc
	v_cndmask_b32_e32 v127, v203, v79, vcc
	v_cndmask_b32_e32 v230, v203, v15, vcc
	s_mov_b64 s[74:75], -1

.LBB0_909:
	s_setprio 1
	v_add_u32_e32 v170, s94, v215
	v_add_u32_e32 v92, v170, v216
	ds_read_b128 v[80:83], v92 offset:0
	ds_read_b128 v[84:87], v92 offset:0x1000
	ds_read_b128 v[88:91], v92 offset:0x2000
	ds_read_b128 v[92:95], v92 offset:0x3000
	v_add_u32_e32 v171, v170, v217
	s_waitcnt lgkmcnt(3)
	s_cmp_gt_i32 s96, -1
	v_mfma_f32_32x32x16_bf16 v[48:63], v[80:83], v[76:79], v[48:63]
	v_add_f32_e32 v246, v96, v112
	ds_read_b128 v[80:83], v171 offset:0
	s_waitcnt lgkmcnt(3)
	s_cselect_b64 s[80:81], -1, 0
	s_cmp_lt_i32 s96, 0
	s_cselect_b64 s[88:89], -1, 0
	s_and_b64 vcc, exec, s[88:89]
	v_mfma_f32_32x32x16_bf16 v[32:47], v[84:87], v[76:79], v[32:47]
	v_add_f32_e32 v248, v97, v113
	v_add_f32_e32 v246, v248, v246
	ds_read_b128 v[84:87], v171 offset:0x1000
	s_waitcnt lgkmcnt(3)
	s_nop 0
	v_mfma_f32_32x32x16_bf16 v[16:31], v[88:91], v[76:79], v[16:31]
	v_add_f32_e32 v247, v98, v114
	v_add_f32_e32 v246, v247, v246
	ds_read_b128 v[88:91], v171 offset:0x2000
	s_waitcnt lgkmcnt(3)
	s_nop 0
	v_mfma_f32_32x32x16_bf16 v[0:15], v[92:95], v[76:79], v[0:15]
	v_add_f32_e32 v248, v99, v115
	v_add_f32_e32 v246, v248, v246
	ds_read_b128 v[76:79], v171 offset:0x3000
	s_waitcnt lgkmcnt(3)
	v_add_u32_e32 v92, v170, v218
	v_mfma_f32_32x32x16_bf16 v[48:63], v[80:83], v[72:75], v[48:63]
	v_add_f32_e32 v247, v100, v116
	v_add_f32_e32 v246, v247, v246
	ds_read_b128 v[80:83], v92 offset:0
	s_waitcnt lgkmcnt(3)
	s_nop 0
	v_mfma_f32_32x32x16_bf16 v[32:47], v[84:87], v[72:75], v[32:47]
	v_add_f32_e32 v248, v101, v117
	v_add_f32_e32 v246, v248, v246
	ds_read_b128 v[84:87], v92 offset:0x1000
	s_waitcnt lgkmcnt(3)
	s_nop 0
	v_mfma_f32_32x32x16_bf16 v[16:31], v[88:91], v[72:75], v[16:31]
	v_add_f32_e32 v247, v102, v118
	v_add_f32_e32 v246, v247, v246
	ds_read_b128 v[88:91], v92 offset:0x2000
	s_waitcnt lgkmcnt(3)
	s_nop 0
	v_mfma_f32_32x32x16_bf16 v[0:15], v[76:79], v[72:75], v[0:15]
	v_add_f32_e32 v248, v103, v119
	v_add_f32_e32 v246, v248, v246
	ds_read_b128 v[72:75], v92 offset:0x3000
	s_waitcnt lgkmcnt(3)
	v_add_u32_e32 v92, v170, v219
	ds_read_b128 v[76:79], v92 offset:0
	s_waitcnt lgkmcnt(3)
	v_mfma_f32_32x32x16_bf16 v[48:63], v[80:83], v[68:71], v[48:63]
	v_add_f32_e32 v247, v104, v120
	v_add_f32_e32 v246, v247, v246
	ds_read_b128 v[80:83], v92 offset:0x1000
	s_waitcnt lgkmcnt(3)
	v_mfma_f32_32x32x16_bf16 v[32:47], v[84:87], v[68:71], v[32:47]
	v_add_f32_e32 v248, v105, v121
	v_add_f32_e32 v246, v248, v246
	ds_read_b128 v[84:87], v92 offset:0x2000
	s_waitcnt lgkmcnt(3)
	v_mfma_f32_32x32x16_bf16 v[16:31], v[88:91], v[68:71], v[16:31]
	v_add_f32_e32 v247, v106, v122
	v_add_f32_e32 v246, v247, v246
	v_mfma_f32_32x32x16_bf16 v[0:15], v[72:75], v[68:71], v[0:15]
	v_add_f32_e32 v248, v107, v123
	v_add_f32_e32 v246, v248, v246
	ds_read_b128 v[68:71], v92 offset:0x3000
	s_waitcnt lgkmcnt(3)
	s_waitcnt lgkmcnt(2)
	s_waitcnt lgkmcnt(1)
	s_nop 0
	s_waitcnt lgkmcnt(0)
	v_mfma_f32_32x32x16_bf16 v[48:63], v[76:79], v[64:67], v[48:63]
	v_add_f32_e32 v247, v108, v124
	v_add_f32_e32 v246, v247, v246
	v_mfma_f32_32x32x16_bf16 v[32:47], v[80:83], v[64:67], v[32:47]
	v_add_f32_e32 v248, v109, v125
	v_add_f32_e32 v246, v248, v246
	v_mfma_f32_32x32x16_bf16 v[16:31], v[84:87], v[64:67], v[16:31]
	v_add_f32_e32 v247, v110, v126
	v_add_f32_e32 v246, v247, v246
	v_mfma_f32_32x32x16_bf16 v[0:15], v[68:71], v[64:67], v[0:15]
	v_add_f32_e32 v248, v111, v127
	v_add_f32_e32 v246, v248, v246
	s_cbranch_vccnz .LBB0_911
	s_add_i32 s94, s94, 0x8000
	s_and_b32 s94, s94, 0x18000
	v_add_u32_e32 v170, s94, v167
	v_add_u32_e32 v68, v170, v207
	ds_read_b128 v[64:67], v68 offset:0
	ds_read_b128 v[80:83], v68 offset:0x2000
	v_add_u32_e32 v68, v170, v208
	ds_read_b128 v[182:185], v68 offset:0
	ds_read_b128 v[220:223], v68 offset:0x2000
	s_waitcnt lgkmcnt(3)
	v_add_u32_e32 v171, v170, v209
	ds_read_b128 v[224:227], v171 offset:0
	v_mfma_f32_32x32x16_bf16 v[64:79], v[64:67], v[128:131], 0
	s_waitcnt lgkmcnt(3)
	ds_read_b128 v[228:231], v171 offset:0x2000
	s_waitcnt lgkmcnt(3)
	v_add_u32_e32 v171, v170, v210
	v_mfma_f32_32x32x16_bf16 v[80:95], v[80:83], v[128:131], 0
	v_mfma_f32_32x32x16_bf16 v[64:79], v[182:185], v[132:135], v[64:79]
	ds_read_b128 v[182:185], v171 offset:0
	s_waitcnt lgkmcnt(3)
	s_nop 0
	v_mfma_f32_32x32x16_bf16 v[80:95], v[220:223], v[132:135], v[80:95]
	ds_read_b128 v[220:223], v171 offset:0x2000
	s_waitcnt lgkmcnt(3)
	v_add_u32_e32 v171, v170, v211
	v_mfma_f32_32x32x16_bf16 v[64:79], v[224:227], v[136:139], v[64:79]
	ds_read_b128 v[224:227], v171 offset:0
	s_waitcnt lgkmcnt(3)
	s_nop 0
	v_mfma_f32_32x32x16_bf16 v[80:95], v[228:231], v[136:139], v[80:95]
	ds_read_b128 v[228:231], v171 offset:0x2000
	s_waitcnt lgkmcnt(3)
	v_add_u32_e32 v171, v170, v212
	v_mfma_f32_32x32x16_bf16 v[64:79], v[182:185], v[140:143], v[64:79]
	ds_read_b128 v[182:185], v171 offset:0
	s_waitcnt lgkmcnt(3)
	s_nop 0
	v_mfma_f32_32x32x16_bf16 v[80:95], v[220:223], v[140:143], v[80:95]
	ds_read_b128 v[220:223], v171 offset:0x2000
	s_waitcnt lgkmcnt(3)
	v_add_u32_e32 v171, v170, v213
	v_add_u32_e32 v170, v170, v214
	v_mfma_f32_32x32x16_bf16 v[64:79], v[224:227], v[144:147], v[64:79]
	ds_read_b128 v[224:227], v171 offset:0
	s_waitcnt lgkmcnt(3)
	s_nop 0
	v_mfma_f32_32x32x16_bf16 v[80:95], v[228:231], v[144:147], v[80:95]
	ds_read_b128 v[228:231], v171 offset:0x2000
	s_waitcnt lgkmcnt(3)
	s_nop 0
	v_mfma_f32_32x32x16_bf16 v[64:79], v[182:185], v[148:151], v[64:79]
	ds_read_b128 v[182:185], v170 offset:0
	s_waitcnt lgkmcnt(3)
	s_nop 0
	v_mfma_f32_32x32x16_bf16 v[80:95], v[220:223], v[148:151], v[80:95]
	ds_read_b128 v[220:223], v170 offset:0x2000
	s_waitcnt lgkmcnt(3)
	s_waitcnt lgkmcnt(2)
	s_waitcnt lgkmcnt(1)
	s_nop 0
	s_waitcnt lgkmcnt(0)
	v_mfma_f32_32x32x16_bf16 v[64:79], v[224:227], v[152:155], v[64:79]
	v_mfma_f32_32x32x16_bf16 v[80:95], v[228:231], v[152:155], v[80:95]
	v_mfma_f32_32x32x16_bf16 v[64:79], v[182:185], v[156:159], v[64:79]
	v_mfma_f32_32x32x16_bf16 v[80:95], v[220:223], v[156:159], v[80:95]
	s_setprio 0
	s_and_b64 vcc, exec, s[0:1]
	s_cbranch_vccz .LBB0_912
	s_branch .LBB0_916

.LBB0_916:
	s_barrier
	v_add_f32_e32 v164, v164, v246
	s_andn2_b64 vcc, exec, s[80:81]
	s_cbranch_vccnz .LBB0_897
	s_cmp_lg_u32 s96, s66
	s_cbranch_scc0 .LBB0_922
	v_mov_b64_e32 v[110:111], v[94:95]
	v_mov_b64_e32 v[126:127], v[78:79]
	s_mov_b64 s[90:91], 0
	s_cmp_eq_u32 s96, s97
	s_mov_b64 s[80:81], 0
	v_mov_b64_e32 v[108:109], v[92:93]
	v_mov_b64_e32 v[106:107], v[90:91]
	v_mov_b64_e32 v[104:105], v[88:89]
	v_mov_b64_e32 v[102:103], v[86:87]
	v_mov_b64_e32 v[100:101], v[84:85]
	v_mov_b64_e32 v[98:99], v[82:83]
	v_mov_b64_e32 v[96:97], v[80:81]
	v_mov_b64_e32 v[124:125], v[76:77]
	v_mov_b64_e32 v[122:123], v[74:75]
	v_mov_b64_e32 v[120:121], v[72:73]
	v_mov_b64_e32 v[118:119], v[70:71]
	v_mov_b64_e32 v[116:117], v[68:69]
	v_mov_b64_e32 v[114:115], v[66:67]
	v_mov_b64_e32 v[112:113], v[64:65]
	s_cbranch_scc0 .LBB0_920
	v_readlane_b32 s80, v255, 32
	v_readlane_b32 s81, v255, 33
	v_cndmask_b32_e64 v112, v203, v64, s[72:73]
	v_cndmask_b32_e64 v96, v203, v80, s[4:5]
	v_cndmask_b32_e64 v113, v65, v203, s[6:7]
	v_cndmask_b32_e64 v97, v81, v203, s[8:9]
	v_cndmask_b32_e64 v114, v203, v66, s[10:11]
	v_cndmask_b32_e64 v98, v203, v82, s[12:13]
	v_cndmask_b32_e64 v115, v203, v67, s[14:15]
	v_cndmask_b32_e64 v99, v203, v83, s[16:17]
	v_cndmask_b32_e64 v116, v203, v68, s[18:19]
	v_cndmask_b32_e64 v100, v203, v84, s[20:21]
	v_cndmask_b32_e64 v117, v203, v69, s[22:23]
	v_cndmask_b32_e64 v101, v203, v85, s[24:25]
	v_cndmask_b32_e64 v118, v203, v70, s[26:27]
	v_cndmask_b32_e64 v102, v203, v86, s[28:29]
	v_cndmask_b32_e64 v119, v203, v71, s[30:31]
	v_cndmask_b32_e64 v103, v203, v87, s[34:35]
	v_cndmask_b32_e64 v120, v203, v72, s[36:37]
	v_cndmask_b32_e64 v104, v203, v88, s[38:39]
	v_cndmask_b32_e64 v121, v203, v73, s[40:41]
	v_cndmask_b32_e64 v105, v203, v89, s[42:43]
	v_cndmask_b32_e64 v122, v203, v74, s[44:45]
	v_cndmask_b32_e64 v106, v203, v90, s[46:47]
	v_cndmask_b32_e64 v123, v203, v75, s[48:49]
	v_cndmask_b32_e64 v107, v203, v91, s[50:51]
	v_cndmask_b32_e64 v124, v203, v76, s[52:53]
	v_cndmask_b32_e64 v108, v203, v92, s[54:55]
	v_cndmask_b32_e64 v125, v203, v77, s[56:57]
	v_cndmask_b32_e64 v109, v203, v93, s[58:59]
	v_cndmask_b32_e64 v126, v203, v78, s[60:61]
	v_cndmask_b32_e64 v110, v203, v94, s[62:63]
	v_mov_b32_e32 v111, v95
	v_cndmask_b32_e64 v127, v203, v79, s[64:65]
	s_and_b64 s[80:81], s[80:81], exec
